# v37 plus one static s_setprio 1 for waves 0-3 (the other half) in the dilated-attention and MoBA item loops
# speedup vs baseline: 1.0007x; 1.0007x over previous
.LBB0_232:
	v_readlane_b32 s0, v253, 56
	v_readlane_b32 s1, v253, 57
	s_andn2_b64 vcc, exec, s[0:1]
	s_cbranch_vccnz .LBB0_273
	s_ashr_i32 s0, s3, 1
	s_and_b32 s3, s0, 0xffffffe0
	s_add_u32 s12, s14, 0xe020000
	s_addc_u32 s13, s15, 0
	s_add_i32 s1, s3, 0x80
	v_and_b32_e32 v2, 63, v155
	v_and_b32_e32 v160, 31, v155
	s_add_u32 s11, s14, 0x28060000
	v_bfe_u32 v3, v155, 5, 1
	v_or_b32_e32 v4, s1, v160
	s_movk_i32 s16, 0x48
	v_lshlrev_b32_e32 v6, 2, v2
	s_addc_u32 s26, s15, 0
	v_lshlrev_b32_e32 v0, 3, v3
	v_mul_lo_u32 v4, v4, s16
	v_xor_b32_e32 v161, 0x80, v6
	s_add_u32 s27, s14, 0x2e060000
	v_mov_b32_e32 v6, 0x3080
	s_movk_i32 s17, 0x184
	v_cmp_gt_u32_e64 s[40:41], 32, v2
	s_addc_u32 s28, s15, 0
	v_add_lshl_u32 v2, v4, v0, 1
	s_add_i32 s14, s3, 0x60
	v_mul_u32_u24_e32 v4, 0x184, v160
	v_mad_u32_u24 v6, v160, s17, v6
	v_mov_b32_e32 v21, s0
	s_movk_i32 s0, 0xffe0
	v_lshlrev_b32_e32 v154, 2, v3
	v_or_b32_e32 v3, s14, v160
	s_add_i32 s15, s3, 0x90
	v_add_lshl_u32 v8, s1, v6, 1
	v_add_lshl_u32 v10, s1, v4, 1
	s_add_i32 s1, s3, 64
	v_add_lshl_u32 v12, s14, v4, 1
	v_add_lshl_u32 v14, s14, v6, 1
	s_add_i32 s14, s3, 32
	v_bfi_b32 v21, s0, v21, v155
	s_add_i32 s0, s3, 48
	v_add_lshl_u32 v7, s15, v6, 1
	v_add_lshl_u32 v9, s15, v4, 1
	v_or_b32_e32 v11, s1, v160
	s_add_i32 s15, s3, 0x70
	v_or_b32_e32 v16, s14, v160
	v_add_lshl_u32 v23, s0, v4, 1
	v_add_lshl_u32 v25, s0, v6, 1
	s_add_i32 s0, s3, 0x7fffffe0
	v_mul_lo_u32 v3, v3, s16
	v_mul_lo_u32 v11, v11, s16
	v_add_lshl_u32 v13, s15, v4, 1
	v_add_lshl_u32 v15, s15, v6, 1
	v_mul_lo_u32 v16, v16, s16
	s_add_i32 s15, s3, 0x50
	v_mul_lo_u32 v21, v21, s16
	v_or_b32_e32 v26, s0, v160
	s_or_b32 s0, s3, 16
	v_add_u32_e32 v5, 0, v0
	v_add_lshl_u32 v3, v3, v0, 1
	v_add_lshl_u32 v11, v11, v0, 1
	v_add_lshl_u32 v16, v16, v0, 1
	v_add_lshl_u32 v17, s1, v4, 1
	v_add_lshl_u32 v18, s15, v4, 1
	v_add_lshl_u32 v19, s1, v6, 1
	v_add_lshl_u32 v20, s15, v6, 1
	v_add_lshl_u32 v21, v21, v0, 1
	v_add_lshl_u32 v22, s14, v4, 1
	v_add_lshl_u32 v24, s14, v6, 1
	v_mul_lo_u32 v26, v26, s16
	v_add_lshl_u32 v27, s0, v6, 1
	v_add_lshl_u32 v6, s3, v6, 1
	v_add_lshl_u32 v28, s0, v4, 1
	v_add_lshl_u32 v4, s3, v4, 1
	v_add_lshl_u32 v26, v26, v0, 1
	v_add_u32_e32 v162, 0, v2
	v_add_u32_e32 v163, 0, v3
	v_add_u32_e32 v2, v5, v7
	v_add_u32_e32 v3, v5, v8
	v_add_u32_e32 v7, v5, v9
	v_add_u32_e32 v8, v5, v10
	v_add_u32_e32 v164, 0, v11
	v_add_u32_e32 v9, v5, v12
	v_add_u32_e32 v10, v5, v13
	v_add_u32_e32 v11, v5, v14
	v_add_u32_e32 v12, v5, v15
	v_add_u32_e32 v165, 0, v16
	v_add_u32_e32 v13, v5, v17
	v_add_u32_e32 v14, v5, v18
	v_add_u32_e32 v15, v5, v19
	v_add_u32_e32 v16, v5, v20
	v_add_u32_e32 v166, 0, v21
	v_add_u32_e32 v17, v5, v22
	v_add_u32_e32 v18, v5, v23
	v_add_u32_e32 v19, v5, v24
	v_add_u32_e32 v20, v5, v25
	v_add_u32_e32 v21, v5, v27
	v_add_u32_e32 v6, v5, v6
	v_add_u32_e32 v22, v5, v28
	v_add_u32_e32 v4, v5, v4
	v_readlane_b32 s0, v254, 32
	s_lshl_b32 s29, s2, 8
	v_lshlrev_b32_e32 v0, 1, v0
	v_add_u32_e32 v167, 0, v26
	v_lshlrev_b32_e32 v156, 1, v154
	v_add_u32_e32 v168, 0xd800, v2
	v_add_u32_e32 v169, 0xd800, v3
	v_add_u32_e32 v170, 0xd800, v7
	v_add_u32_e32 v171, 0xd800, v8
	v_add_u32_e32 v172, 0xd800, v9
	v_add_u32_e32 v173, 0xd800, v10
	v_add_u32_e32 v174, 0xd800, v11
	v_add_u32_e32 v175, 0xd800, v12
	v_add_u32_e32 v176, 0xd800, v13
	v_add_u32_e32 v177, 0xd800, v14
	v_add_u32_e32 v178, 0xd800, v15
	v_add_u32_e32 v179, 0xd800, v16
	v_add_u32_e32 v180, 0xd800, v17
	v_add_u32_e32 v181, 0xd800, v18
	v_add_u32_e32 v182, 0xd800, v19
	v_add_u32_e32 v183, 0xd800, v20
	v_add_u32_e32 v184, 0xd800, v21
	v_add_u32_e32 v185, 0xd800, v6
	v_add_u32_e32 v186, 0xd800, v22
	v_add_u32_e32 v187, 0xd800, v4
	v_readlane_b32 s30, v253, 58
	s_mov_b32 s33, s0
	v_readlane_b32 s1, v254, 33
	v_readlane_b32 s36, v253, 0
	s_cmp_ge_u32 s36, 0x100
	s_cbranch_scc1 .Lprio_0
	s_setprio 1

.LBB0_628:
	v_readlane_b32 s0, v254, 6
	v_readlane_b32 s1, v254, 7
	s_andn2_b64 vcc, exec, s[0:1]
	s_cbranch_vccnz .LBB0_819
	v_readlane_b32 s0, v254, 41
	v_readlane_b32 s2, v253, 0
	s_nop 0
	v_mov_b32_e32 v0, s0
	s_waitcnt vmcnt(0)
	ds_read_b64 v[2:3], v0
	v_mbcnt_lo_u32_b32 v0, -1, 0
	v_mbcnt_hi_u32_b32 v0, -1, v0
	s_waitcnt lgkmcnt(0)
	v_readfirstlane_b32 s0, v2
	v_add_u32_e32 v2, s2, v0
	v_readlane_b32 s2, v254, 2
	v_readlane_b32 s3, v254, 3
	v_readfirstlane_b32 s1, v3
	s_and_b64 vcc, exec, s[2:3]
	s_cbranch_vccz .LBB0_819
	v_and_b32_e32 v3, 63, v2
	v_lshlrev_b32_e32 v0, 3, v2
	v_ashrrev_i32_e32 v9, 3, v2
	s_movk_i32 s11, 0x48
	v_and_b32_e32 v4, 56, v0
	v_cmp_eq_u32_e64 s[42:43], 0, v3
	v_lshlrev_b32_e32 v12, 2, v3
	v_cmp_gt_u32_e64 s[44:45], 32, v3
	s_movk_i32 s16, 0x1800
	v_mul_lo_u32 v3, v9, s11
	v_lshlrev_b32_e32 v10, 2, v9
	v_mad_i64_i32 v[136:137], s[14:15], v9, s16, 0
	v_add_lshl_u32 v9, v3, v4, 1
	v_add_u32_e32 v3, 0x200, v2
	v_ashrrev_i32_e32 v3, 3, v3
	v_mad_i64_i32 v[138:139], s[14:15], v3, s16, 0
	v_mul_lo_u32 v3, v3, s11
	v_xor_b32_e32 v164, 0x80, v12
	v_add_lshl_u32 v12, v3, v4, 1
	v_add_u32_e32 v3, 0x400, v2
	v_ashrrev_i32_e32 v3, 3, v3
	v_mad_i64_i32 v[140:141], s[14:15], v3, s16, 0
	v_mul_lo_u32 v3, v3, s11
	v_add_lshl_u32 v13, v3, v4, 1
	v_add_u32_e32 v3, 0x600, v2
	v_ashrrev_i32_e32 v3, 3, v3
	v_mad_i64_i32 v[142:143], s[14:15], v3, s16, 0
	v_mul_lo_u32 v3, v3, s11
	v_add_lshl_u32 v14, v3, v4, 1
	v_or_b32_e32 v3, 1, v10
	v_mad_i64_i32 v[146:147], s[14:15], v3, s16, 0
	v_or_b32_e32 v3, 2, v10
	v_mad_i64_i32 v[148:149], s[14:15], v3, s16, 0
	v_or_b32_e32 v3, 3, v10
	v_add_u32_e32 v11, 0x104, v10
	v_mad_i64_i32 v[150:151], s[14:15], v3, s16, 0
	v_mul_u32_u24_e32 v3, 0x104, v4
	v_add_lshl_u32 v15, v3, v10, 1
	v_add_lshl_u32 v16, v3, v11, 1
	v_mov_b32_e32 v3, 0x208
	s_movk_i32 s11, 0x104
	s_add_u32 s2, s0, 0x45be0a00
	v_mad_u32_u24 v3, v4, s11, v3
	s_addc_u32 s3, s1, 0
	v_add_lshl_u32 v17, v3, v10, 1
	v_add_lshl_u32 v18, v3, v11, 1
	v_mov_b32_e32 v3, 0x410
	s_add_u32 s8, s0, 0xe020000
	v_mad_u32_u24 v3, v4, s11, v3
	v_bfe_u32 v8, v2, 5, 1
	s_addc_u32 s9, s1, 0
	v_add_lshl_u32 v19, v3, v10, 1
	v_add_lshl_u32 v20, v3, v11, 1
	v_mov_b32_e32 v3, 0x618
	v_lshlrev_b32_e32 v0, 3, v8
	s_add_u32 s12, s0, 0x4dce0a00
	v_mad_u32_u24 v3, v4, s11, v3
	v_and_b32_e32 v5, 31, v2
	v_cmp_eq_u32_e64 s[40:41], 0, v2
	v_add_u32_e32 v162, 0x100, v2
	v_lshlrev_b64 v[6:7], v2, -1
	s_addc_u32 s13, s1, 0
	v_mad_i64_i32 v[144:145], s[14:15], v10, s16, 0
	v_add_lshl_u32 v10, v3, v10, 1
	v_add_lshl_u32 v11, v3, v11, 1
	v_add_u32_e32 v165, 0x300, v2
	v_add_u32_e32 v166, 0x500, v2
	v_add_u32_e32 v167, 0x700, v2
	v_add_u32_e32 v168, 0x900, v2
	v_add_u32_e32 v169, 0xb00, v2
	v_add_u32_e32 v170, 0xd00, v2
	v_add_u32_e32 v171, 0xf00, v2
	v_add_u32_e32 v172, 0x1100, v2
	v_add_u32_e32 v173, 0x1300, v2
	v_add_u32_e32 v174, 0x1500, v2
	v_add_u32_e32 v175, 0x1700, v2
	v_add_u32_e32 v176, 0x1900, v2
	v_add_u32_e32 v177, 0x1b00, v2
	v_add_u32_e32 v178, 0x1d00, v2
	v_add_u32_e32 v179, 0x1f00, v2
	v_lshl_add_u64 v[2:3], s[0:1], 0, v[0:1]
	s_mov_b64 s[0:1], 0x45ce0a00
	v_not_b32_e32 v133, v7
	v_not_b32_e32 v132, v6
	v_lshlrev_b32_e32 v6, 4, v8
	v_mov_b32_e32 v7, v1
	v_mul_u32_u24_e32 v21, 0x104, v5
	v_lshl_add_u64 v[152:153], v[2:3], 0, s[0:1]
	v_mul_u32_u24_e32 v2, 0x90, v5
	v_readlane_b32 s0, v254, 46
	v_lshl_add_u64 v[134:135], s[8:9], 0, v[6:7]
	v_mul_u32_u24_e32 v7, 0x48, v5
	v_add3_u32 v181, v2, v6, s0
	v_lshlrev_b32_e32 v2, 1, v21
	v_readlane_b32 s0, v254, 47
	v_lshlrev_b32_e32 v8, 2, v8
	v_add_lshl_u32 v7, v0, v7, 1
	s_movk_i32 s11, 0x2000
	v_add3_u32 v183, v0, v2, s0
	v_readlane_b32 s0, v254, 32
	v_or_b32_e32 v163, 0xffffff00, v5
	v_or_b32_e32 v180, 0xe0, v5
	v_cmp_gt_i32_e64 s[46:47], s11, v179
	v_sub_u32_e32 v182, 0, v8
	v_lshlrev_b32_e32 v154, 1, v4
	v_add_u32_e32 v184, 0, v9
	v_add_u32_e32 v185, 0, v12
	v_add_u32_e32 v186, 0, v13
	v_add_u32_e32 v187, 0, v14
	v_add_u32_e32 v188, 0, v15
	v_add_u32_e32 v189, 0, v16
	v_add_u32_e32 v190, 0, v17
	v_add_u32_e32 v191, 0, v18
	v_add_u32_e32 v192, 0, v19
	v_add_u32_e32 v193, 0, v20
	v_add_u32_e32 v194, 0, v10
	v_add_u32_e32 v195, 0, v11
	v_add_u32_e32 v196, 0, v7
	s_mov_b32 s11, s0
	v_readlane_b32 s1, v254, 33
	v_readlane_b32 s36, v253, 0
	s_cmp_ge_u32 s36, 0x100
	s_cbranch_scc1 .Lprio_1
	s_setprio 1
